# combine phase: final-norm gain vectors loaded once before the token loop instead of a 16-byte load plus vmcnt(0) between consecutive output stores (each wait also drained the previous nt store)
# speedup vs baseline: 1.0665x; 1.0071x over previous
.LBB0_1393:
	s_cmp_lt_i32 s28, 10
	s_cselect_b64 s[2:3], -1, 0
	s_and_b64 s[0:1], s[2:3], s[0:1]
	s_andn2_b64 vcc, exec, s[0:1]
	s_cbranch_vccnz .LBB0_1399
	v_readlane_b32 s0, v255, 8
	s_lshl_b32 s0, s0, 3
	v_readlane_b32 s1, v255, 18
	s_add_i32 s2, s0, s1
	s_cmpk_gt_i32 s2, 0x3fff
	s_cbranch_scc1 .LBB0_1399
	v_mbcnt_lo_u32_b32 v0, -1, 0
	v_mbcnt_hi_u32_b32 v4, -1, v0
	v_and_b32_e32 v0, 64, v4
	v_add_u32_e32 v0, 64, v0
	v_xor_b32_e32 v1, 1, v4
	v_cmp_lt_i32_e32 vcc, v1, v0
	v_readlane_b32 s15, v255, 2
	s_lshl_b32 s33, s15, 3
	v_cndmask_b32_e32 v1, v4, v1, vcc
	v_lshlrev_b32_e32 v28, 2, v1
	v_xor_b32_e32 v1, 2, v4
	v_cmp_lt_i32_e32 vcc, v1, v0
	s_add_i32 s6, s2, s33
	s_ashr_i32 s7, s6, 31
	v_cndmask_b32_e32 v1, v4, v1, vcc
	v_lshlrev_b32_e32 v29, 2, v1
	v_xor_b32_e32 v1, 4, v4
	v_cmp_lt_i32_e32 vcc, v1, v0
	s_lshl_b32 s4, s15, 4
	s_lshl_b64 s[6:7], s[6:7], 12
	v_cndmask_b32_e32 v1, v4, v1, vcc
	v_lshlrev_b32_e32 v30, 2, v1
	v_xor_b32_e32 v1, 8, v4
	v_cmp_lt_i32_e32 vcc, v1, v0
	v_mov_b32_e32 v9, 0
	s_add_u32 s6, s58, s6
	v_cndmask_b32_e32 v1, v4, v1, vcc
	v_lshlrev_b32_e32 v31, 2, v1
	v_xor_b32_e32 v1, 16, v4
	v_cmp_lt_i32_e32 vcc, v1, v0
	s_addc_u32 s7, s59, s7
	s_ashr_i32 s5, s4, 31
	v_cndmask_b32_e32 v1, v4, v1, vcc
	v_lshlrev_b32_e32 v32, 2, v1
	v_xor_b32_e32 v1, 32, v4
	v_cmp_lt_i32_e32 vcc, v1, v0
	s_ashr_i32 s3, s2, 31
	s_mov_b64 s[0:1], 0x8800000
	v_cndmask_b32_e32 v0, v4, v1, vcc
	v_lshlrev_b32_e32 v33, 2, v0
	v_lshlrev_b32_e32 v0, 3, v4
	v_mov_b32_e32 v1, v9
	v_lshl_add_u64 v[2:3], s[90:91], 0, v[0:1]
	s_lshl_b64 s[8:9], s[4:5], 12
	s_lshl_b64 s[10:11], s[2:3], 12
	v_lshl_add_u64 v[12:13], v[2:3], 0, s[0:1]
	v_lshlrev_b32_e32 v2, 2, v4
	v_mov_b32_e32 v3, v9
	s_add_u32 s10, s58, s10
	v_lshl_add_u64 v[14:15], s[12:13], 0, v[2:3]
	s_addc_u32 s11, s59, s11
	s_lshl_b64 s[12:13], s[2:3], 11
	s_add_u32 s12, s90, s12
	s_addc_u32 s13, s91, s13
	v_lshl_add_u64 v[0:1], s[12:13], 0, v[0:1]
	v_lshl_add_u64 v[16:17], v[0:1], 0, s[0:1]
	v_readlane_b32 s0, v255, 8
	v_readlane_b32 s1, v255, 18
	s_lshl_b32 s0, s0, 5
	s_lshl_b32 s1, s1, 2
	v_lshlrev_b32_e32 v8, 4, v4
	s_add_i32 s0, s0, s1
	v_lshl_add_u64 v[10:11], s[56:57], 0, v[8:9]
	s_lshl_b64 s[12:13], s[4:5], 11
	s_or_b32 s14, s0, 3
	s_lshl_b32 s3, s15, 6
	s_add_i32 s5, 0, 0x20400
	v_mov_b32_e32 v34, 0x3727c5ac
	s_mov_b32 s38, 0xf800000
	v_mov_b32_e32 v35, 0x260
	global_load_dwordx4 v[200:203], v[10:11], off
	global_load_dwordx4 v[204:207], v[10:11], off offset:1024
	global_load_dwordx4 v[208:211], v[10:11], off offset:2048
	global_load_dwordx4 v[212:215], v[10:11], off offset:3072
	s_waitcnt vmcnt(0)
	s_branch .LBB0_1397

.LBB0_1397:
	s_add_i32 s39, s33, s2
	s_cmpk_lt_i32 s39, 0x4000
	s_cselect_b32 s16, s39, s2
	s_lshl_b32 s18, s16, 2
	s_ashr_i32 s17, s16, 31
	s_ashr_i32 s19, s18, 31
	s_lshl_b64 s[0:1], s[16:17], 11
	s_lshl_b64 s[16:17], s[18:19], 2
	s_add_u32 s22, s40, s16
	s_addc_u32 s23, s41, s17
	s_add_u32 s20, s44, s16
	s_addc_u32 s21, s45, s17
	s_add_u32 s16, s36, s16
	s_addc_u32 s17, s37, s17
	s_or_b32 s18, s18, 2
	s_ashr_i32 s19, s18, 31
	s_lshl_b64 s[18:19], s[18:19], 2
	s_add_u32 s18, s36, s18
	s_addc_u32 s19, s37, s19
	s_ashr_i32 s15, s14, 31
	global_load_dwordx4 v[0:3], v9, s[22:23]
	s_add_i32 s30, s14, -3
	s_lshl_b64 s[22:23], s[14:15], 2
	s_add_u32 s34, s44, s22
	s_addc_u32 s35, s45, s23
	s_add_u32 s26, s40, s22
	s_addc_u32 s27, s41, s23
	s_add_i32 s24, s14, -1
	s_ashr_i32 s25, s24, 31
	s_lshl_b64 s[24:25], s[24:25], 2
	s_add_u32 s42, s44, s24
	s_addc_u32 s43, s45, s25
	s_add_u32 s28, s40, s24
	s_addc_u32 s29, s41, s25
	global_load_dword v19, v9, s[26:27]
	global_load_dword v25, v9, s[28:29]
	s_add_i32 s26, s14, -2
	s_ashr_i32 s27, s26, 31
	s_lshl_b64 s[26:27], s[26:27], 2
	s_add_u32 s28, s44, s26
	s_addc_u32 s29, s45, s27
	s_add_u32 s46, s40, s26
	s_addc_u32 s47, s41, s27
	global_load_dword v38, v9, s[46:47]
	global_load_dword v39, v9, s[42:43]
	global_load_dword v40, v9, s[34:35]
	s_ashr_i32 s31, s30, 31
	s_lshl_b64 s[30:31], s[30:31], 2
	s_add_u32 s34, s44, s30
	s_addc_u32 s35, s45, s31
	s_add_u32 s42, s40, s30
	s_addc_u32 s43, s41, s31
	global_load_dword v41, v9, s[42:43]
	global_load_dword v42, v9, s[28:29]
	global_load_dword v43, v9, s[34:35]
	global_load_dwordx2 v[26:27], v[16:17], off offset:1536 nt
	global_load_dwordx2 v[36:37], v[16:17], off offset:1024 nt
	global_load_dwordx2 v[20:21], v[16:17], off offset:512 nt
	global_load_dwordx4 v[4:7], v9, s[20:21]
	s_add_u32 s20, s36, s22
	s_addc_u32 s21, s37, s23
	s_add_u32 s22, s36, s24
	s_addc_u32 s23, s37, s25
	global_load_dword v18, v9, s[20:21]
	s_add_u32 s20, s36, s26
	s_addc_u32 s21, s37, s27
	s_add_u32 s24, s36, s30
	s_addc_u32 s25, s37, s31
	global_load_dword v24, v9, s[22:23]
	global_load_dword v22, v9, s[20:21]
	global_load_dword v23, v9, s[24:25]
	s_cmpk_gt_i32 s39, 0x3fff
	s_waitcnt vmcnt(0)
	v_lshlrev_b32_e32 v1, 2, v1
	v_lshlrev_b32_e32 v2, 2, v2
	v_lshlrev_b32_e32 v3, 2, v3
	v_add_u32_e32 v1, s5, v1
	v_add_u32_e32 v2, s5, v2
	v_add_u32_e32 v3, s5, v3
	v_lshlrev_b32_e32 v0, 2, v0
	v_add_u32_e32 v0, s5, v0
	v_lshlrev_b32_e32 v19, 2, v19
	v_lshlrev_b32_e32 v25, 2, v25
	v_add_u32_e32 v19, s5, v19
	v_add_u32_e32 v25, s5, v25
	v_lshlrev_b32_e32 v38, 2, v38
	v_add_u32_e32 v38, s5, v38
	ds_read_b32 v1, v1
	ds_read_b32 v25, v25
	ds_read_b32 v114, v2
	ds_read_b32 v115, v3
	ds_read_b32 v19, v19
	ds_read_b32 v44, v38
	s_waitcnt lgkmcnt(0)
	v_add_u32_e32 v2, v39, v25
	v_ashrrev_i32_e32 v3, 31, v2
	v_lshlrev_b64 v[2:3], 10, v[2:3]
	v_lshl_add_u64 v[38:39], v[14:15], 0, v[2:3]
	global_load_dword v60, v[38:39], off offset:768 nt
	global_load_dword v48, v[38:39], off nt
	global_load_dword v56, v[38:39], off offset:512 nt
	global_load_dword v52, v[38:39], off offset:256 nt
	global_load_dwordx2 v[2:3], v9, s[18:19]
	v_add_u32_e32 v38, v40, v19
	v_ashrrev_i32_e32 v39, 31, v38
	v_lshlrev_b64 v[38:39], 10, v[38:39]
	v_lshlrev_b32_e32 v19, 2, v41
	v_lshl_add_u64 v[38:39], v[14:15], 0, v[38:39]
	v_add_u32_e32 v19, s5, v19
	global_load_dword v64, v[38:39], off nt
	global_load_dword v68, v[38:39], off offset:256 nt
	global_load_dword v72, v[38:39], off offset:512 nt
	ds_read_b32 v19, v19
	v_add_u32_e32 v40, v42, v44
	v_ashrrev_i32_e32 v41, 31, v40
	v_lshlrev_b64 v[40:41], 10, v[40:41]
	v_lshl_add_u64 v[40:41], v[14:15], 0, v[40:41]
	s_waitcnt lgkmcnt(0)
	v_add_u32_e32 v42, v43, v19
	v_ashrrev_i32_e32 v43, 31, v42
	v_lshlrev_b64 v[42:43], 10, v[42:43]
	global_load_dword v74, v[40:41], off offset:768 nt
	v_lshl_add_u64 v[42:43], v[14:15], 0, v[42:43]
	global_load_dword v86, v[42:43], off nt
	global_load_dword v90, v[42:43], off offset:256 nt
	global_load_dword v94, v[42:43], off offset:512 nt
	global_load_dword v98, v[42:43], off offset:768 nt
	global_load_dword v102, v[40:41], off nt
	global_load_dword v106, v[40:41], off offset:256 nt
	global_load_dword v110, v[40:41], off offset:512 nt
	global_load_dword v116, v[38:39], off offset:768 nt
	global_load_dwordx2 v[44:45], v[16:17], off nt
	v_lshlrev_b32_e32 v40, 16, v36
	v_lshlrev_b32_e32 v119, 16, v20
	v_and_b32_e32 v20, 0xffff0000, v20
	v_lshlrev_b32_e32 v38, 16, v26
	v_lshlrev_b32_e32 v42, 16, v37
	v_mov_b32_e32 v25, v22
	v_and_b32_e32 v117, 0xffff0000, v36
	v_mov_b32_e32 v19, v24
	v_and_b32_e32 v39, 0xffff0000, v26
	v_lshlrev_b32_e32 v41, 16, v27
	v_and_b32_e32 v43, 0xffff0000, v27
	v_mov_b32_e32 v27, v22
	v_mov_b32_e32 v26, v23
	v_and_b32_e32 v118, 0xffff0000, v37
	v_mov_b32_e32 v37, v18
	v_mov_b32_e32 v36, v24
	s_waitcnt vmcnt(17)
	v_cvt_pk_f32_fp8_e32 v[58:59], v60
	s_waitcnt vmcnt(16)
	v_cvt_pk_f32_fp8_e32 v[46:47], v48
	s_waitcnt vmcnt(15)
	v_cvt_pk_f32_fp8_e32 v[54:55], v56
	s_waitcnt vmcnt(14)
	v_cvt_pk_f32_fp8_e32 v[50:51], v52
	v_cvt_pk_f32_fp8_sdwa v[52:53], v52 src0_sel:WORD_1
	v_mul_f32_e32 v75, v24, v59
	v_cvt_pk_f32_fp8_sdwa v[56:57], v56 src0_sel:WORD_1
	v_mov_b32_e32 v77, v51
	v_mov_b32_e32 v78, v52
	s_waitcnt vmcnt(12)
	v_cvt_pk_f32_fp8_e32 v[62:63], v64
	s_waitcnt vmcnt(11)
	v_cvt_pk_f32_fp8_e32 v[66:67], v68
	v_cvt_pk_f32_fp8_sdwa v[68:69], v68 src0_sel:WORD_1
	s_waitcnt vmcnt(10)
	v_cvt_pk_f32_fp8_e32 v[70:71], v72
	v_cvt_pk_f32_fp8_sdwa v[72:73], v72 src0_sel:WORD_1
	s_waitcnt vmcnt(8)
	v_cvt_pk_f32_fp8_e32 v[84:85], v86
	s_waitcnt vmcnt(7)
	v_cvt_pk_f32_fp8_e32 v[88:89], v90
	s_waitcnt vmcnt(6)
	v_cvt_pk_f32_fp8_e32 v[92:93], v94
	v_cvt_pk_f32_fp8_sdwa v[90:91], v90 src0_sel:WORD_1
	v_cvt_pk_f32_fp8_sdwa v[94:95], v94 src0_sel:WORD_1
	s_waitcnt vmcnt(3)
	v_cvt_pk_f32_fp8_e32 v[104:105], v106
	v_cvt_pk_f32_fp8_e32 v[80:81], v74
	s_waitcnt vmcnt(2)
	v_cvt_pk_f32_fp8_e32 v[108:109], v110
	v_cvt_pk_f32_fp8_e32 v[96:97], v98
	v_mov_b32_e32 v113, v88
	v_mov_b32_e32 v88, v105
	v_cvt_pk_f32_fp8_e32 v[100:101], v102
	v_cvt_pk_f32_fp8_sdwa v[106:107], v106 src0_sel:WORD_1
	v_cvt_pk_f32_fp8_sdwa v[110:111], v110 src0_sel:WORD_1
	v_pk_mul_f32 v[88:89], v[22:23], v[88:89]
	v_mov_b32_e32 v59, v80
	v_fmac_f32_e32 v40, v23, v92
	v_mov_b32_e32 v112, v104
	v_mov_b32_e32 v92, v109
	v_add_f32_e32 v20, v89, v20
	v_pk_mul_f32 v[58:59], v[24:25], v[58:59]
	v_fmac_f32_e32 v42, v23, v94
	v_fmac_f32_e32 v38, v23, v96
	v_mov_b32_e32 v104, v90
	v_mov_b32_e32 v90, v95
	v_pk_mul_f32 v[94:95], v[22:23], v[112:113]
	v_pk_mul_f32 v[92:93], v[22:23], v[92:93]
	v_add_f32_e32 v20, v88, v20
	s_waitcnt vmcnt(0)
	v_lshlrev_b32_e32 v88, 16, v44
	v_and_b32_e32 v89, 0xffff0000, v44
	v_mov_b32_e32 v44, v23
	v_mov_b32_e32 v79, v68
	v_mov_b32_e32 v68, v53
	v_mov_b32_e32 v52, v71
	v_mov_b32_e32 v53, v55
	v_cvt_pk_f32_fp8_sdwa v[86:87], v86 src0_sel:WORD_1
	v_cvt_pk_f32_fp8_sdwa v[98:99], v98 src0_sel:WORD_1
	v_add_f32_e32 v38, v59, v38
	v_add_f32_e32 v51, v95, v119
	v_add_f32_e32 v55, v93, v117
	v_pk_fma_f32 v[84:85], v[44:45], v[84:85], v[88:89] op_sel_hi:[0,1,1]
	v_cvt_pk_f32_fp8_sdwa v[82:83], v74 src0_sel:WORD_1
	v_pk_mul_f32 v[52:53], v[18:19], v[52:53]
	v_cvt_pk_f32_fp8_sdwa v[102:103], v102 src0_sel:WORD_1
	v_mov_b32_e32 v105, v106
	v_mov_b32_e32 v106, v91
	v_mov_b32_e32 v91, v111
	v_add_f32_e32 v59, v58, v38
	v_add_f32_e32 v38, v94, v51
	v_add_f32_e32 v51, v92, v55
	v_pk_fma_f32 v[84:85], v[22:23], v[100:101], v[84:85] op_sel_hi:[0,1,1]
	v_cvt_pk_f32_fp8_sdwa v[48:49], v48 src0_sel:WORD_1
	v_mov_b32_e32 v76, v67
	v_pk_mul_f32 v[104:105], v[26:27], v[104:105]
	v_pk_mul_f32 v[106:107], v[26:27], v[106:107]
	v_pk_mul_f32 v[26:27], v[26:27], v[90:91]
	v_add_f32_e32 v51, v53, v51
	v_pk_fma_f32 v[46:47], v[24:25], v[46:47], v[84:85] op_sel_hi:[0,1,1]
	v_cvt_pk_f32_fp8_sdwa v[60:61], v60 src0_sel:WORD_1
	v_pk_mul_f32 v[76:77], v[18:19], v[76:77]
	v_add_f32_e32 v26, v26, v118
	v_add_f32_e32 v80, v52, v51
	v_mov_b32_e32 v52, v57
	v_mov_b32_e32 v53, v73
	v_pk_fma_f32 v[62:63], v[18:19], v[62:63], v[46:47] op_sel_hi:[0,1,1]
	v_lshlrev_b32_e32 v46, 16, v45
	v_and_b32_e32 v47, 0xffff0000, v45
	v_pk_mul_f32 v[78:79], v[36:37], v[78:79]
	v_pk_mul_f32 v[68:69], v[36:37], v[68:69]
	v_add_f32_e32 v27, v26, v27
	v_add_f32_e32 v20, v77, v20
	v_pk_mul_f32 v[36:37], v[36:37], v[52:53]
	v_pk_fma_f32 v[44:45], v[44:45], v[86:87], v[46:47] op_sel_hi:[0,1,1]
	v_mov_b32_e32 v109, v98
	v_mov_b32_e32 v111, v99
	v_add_f32_e32 v26, v76, v20
	v_cvt_pk_f32_fp8_sdwa v[52:53], v116 src0_sel:WORD_1
	v_add_f32_e32 v20, v27, v36
	v_pk_fma_f32 v[44:45], v[22:23], v[102:103], v[44:45] op_sel_hi:[0,1,1]
	v_pk_fma_f32 v[40:41], v[22:23], v[108:109], v[40:41]
	v_pk_fma_f32 v[42:43], v[22:23], v[110:111], v[42:43]
	v_mov_b32_e32 v46, v24
	v_mov_b32_e32 v47, v23
	v_mov_b32_e32 v51, v97
	v_mov_b32_e32 v55, v82
	v_mov_b32_e32 v57, v83
	v_add_f32_e32 v90, v20, v37
	v_cvt_pk_f32_fp8_e32 v[36:37], v116
	v_pk_fma_f32 v[44:45], v[24:25], v[48:49], v[44:45] op_sel_hi:[0,1,1]
	v_pk_fma_f32 v[38:39], v[46:47], v[50:51], v[38:39]
	v_pk_fma_f32 v[40:41], v[24:25], v[54:55], v[40:41]
	v_pk_fma_f32 v[24:25], v[24:25], v[56:57], v[42:43]
	v_mov_b32_e32 v42, v18
	v_mov_b32_e32 v43, v22
	v_mov_b32_e32 v67, v81
	v_pk_fma_f32 v[54:55], v[42:43], v[66:67], v[38:39]
	v_mov_b32_e32 v71, v60
	v_pk_fma_f32 v[56:57], v[18:19], v[70:71], v[40:41]
	v_mov_b32_e32 v73, v61
	v_mov_b32_e32 v74, v54
	v_cvt_pk_f32_fp8_sdwa v[64:65], v64 src0_sel:WORD_1
	v_mul_f32_e32 v77, v18, v52
	v_pk_fma_f32 v[60:61], v[18:19], v[72:73], v[24:25]
	v_pk_mul_f32 v[22:23], v[54:55], v[54:55]
	v_pk_add_f32 v[24:25], v[54:55], v[74:75]
	v_mov_b32_e32 v76, v56
	v_mul_f32_e32 v53, v18, v53
	v_mul_f32_e32 v20, v80, v80
	v_mov_b32_e32 v23, v25
	v_mov_b32_e32 v27, v18
	v_mov_b32_e32 v38, v26
	v_mov_b32_e32 v39, v37
	v_pk_add_f32 v[48:49], v[56:57], v[76:77]
	v_mov_b32_e32 v52, v60
	v_mul_f32_e32 v58, v90, v90
	v_pk_fma_f32 v[66:67], v[26:27], v[38:39], v[22:23]
	v_pk_add_f32 v[70:71], v[60:61], v[52:53]
	v_pk_fma_f32 v[22:23], v[56:57], v[56:57], v[20:21]
	v_pk_mul_f32 v[38:39], v[48:49], v[48:49]
	v_pk_mul_f32 v[40:41], v[70:71], v[70:71]
	v_mov_b32_e32 v23, v39
	v_pk_fma_f32 v[38:39], v[60:61], v[60:61], v[58:59]
	v_pk_fma_f32 v[64:65], v[18:19], v[64:65], v[44:45] op_sel_hi:[0,1,1]
	v_mov_b32_e32 v39, v41
	v_pk_mul_f32 v[44:45], v[64:65], v[64:65]
	v_pk_add_f32 v[22:23], v[22:23], v[38:39]
	v_mov_b32_e32 v38, v62
	v_mov_b32_e32 v39, v18
	v_mov_b32_e32 v40, v62
	v_mov_b32_e32 v41, v36
	v_mul_f32_e32 v58, v63, v63
	v_mov_b32_e32 v42, v64
	v_mov_b32_e32 v43, v18
	v_mov_b32_e32 v46, v64
	v_mov_b32_e32 v47, v36
	v_pk_fma_f32 v[72:73], v[38:39], v[40:41], v[58:59]
	v_mov_b32_e32 v58, v45
	v_pk_fma_f32 v[38:39], v[42:43], v[46:47], v[58:59]
	v_lshlrev_b32_e32 v20, 16, v21
	v_pk_add_f32 v[40:41], v[72:73], v[38:39]
	v_pk_mul_f32 v[38:39], v[72:73], v[38:39]
	v_and_b32_e32 v21, 0xffff0000, v21
	v_mov_b32_e32 v41, v39
	v_mov_b32_e32 v38, v104
	v_mov_b32_e32 v39, v106
	v_pk_add_f32 v[20:21], v[38:39], v[20:21]
	v_mov_b32_e32 v106, v105
	v_pk_add_f32 v[20:21], v[20:21], v[106:107]
	v_mov_b32_e32 v38, v78
	v_mov_b32_e32 v39, v68
	v_pk_add_f32 v[20:21], v[20:21], v[38:39]
	v_mov_b32_e32 v68, v79
	v_pk_add_f32 v[58:59], v[20:21], v[68:69]
	v_lshl_add_u64 v[38:39], v[12:13], 0, s[0:1]
	v_pk_mul_f32 v[20:21], v[58:59], v[58:59]
	v_pk_mov_b32 v[18:19], v[58:59], v[18:19] op_sel:[1,0]
	v_mov_b32_e32 v36, v59
	v_mov_b32_e32 v21, v25
	v_pk_fma_f32 v[18:19], v[18:19], v[36:37], v[20:21]
	s_nop 0
	v_pk_add_f32 v[20:21], v[66:67], v[18:19]
	v_pk_mul_f32 v[18:19], v[66:67], v[18:19]
	s_nop 0
	v_mov_b32_e32 v21, v19
	v_pk_add_f32 v[18:19], v[40:41], v[20:21]
	s_nop 0
	v_pk_add_f32 v[18:19], v[18:19], v[22:23]
	ds_read_b32 v22, v0
	v_add_f32_e32 v18, v18, v19
	ds_bpermute_b32 v19, v28, v18
	v_add_u32_e32 v0, v5, v1
	v_ashrrev_i32_e32 v1, 31, v0
	s_waitcnt lgkmcnt(1)
	v_add_u32_e32 v4, v4, v22
	v_ashrrev_i32_e32 v5, 31, v4
	s_waitcnt lgkmcnt(0)
	v_add_f32_e32 v23, v18, v19
	global_load_dwordx2 v[20:21], v9, s[16:17]
	global_load_dwordx2 v[18:19], v9, s[16:17] offset:4
	ds_bpermute_b32 v24, v29, v23
	v_lshlrev_b64 v[36:37], 10, v[4:5]
	v_add_u32_e32 v4, v6, v114
	v_ashrrev_i32_e32 v5, 31, v4
	v_lshlrev_b64 v[68:69], 10, v[4:5]
	s_waitcnt lgkmcnt(0)
	v_add_f32_e32 v23, v23, v24
	ds_bpermute_b32 v27, v30, v23
	v_lshlrev_b64 v[24:25], 10, v[0:1]
	v_add_u32_e32 v0, v7, v115
	v_lshl_add_u64 v[36:37], v[14:15], 0, v[36:37]
	v_lshl_add_u64 v[24:25], v[14:15], 0, v[24:25]
	s_waitcnt lgkmcnt(0)
	v_add_f32_e32 v1, v23, v27
	ds_bpermute_b32 v22, v31, v1
	v_lshl_add_u64 v[68:69], v[14:15], 0, v[68:69]
	s_waitcnt lgkmcnt(0)
	v_add_f32_e32 v6, v1, v22
	ds_bpermute_b32 v7, v32, v6
	v_ashrrev_i32_e32 v1, 31, v0
	v_lshlrev_b64 v[40:41], 10, v[0:1]
	v_lshl_add_u64 v[74:75], v[14:15], 0, v[40:41]
	s_waitcnt lgkmcnt(0)
	v_add_f32_e32 v27, v6, v7
	ds_bpermute_b32 v42, v33, v27
	global_load_dwordx2 v[4:5], v[38:39], off nt
	global_load_dwordx2 v[0:1], v[38:39], off offset:512 nt
	global_load_dwordx2 v[6:7], v[38:39], off offset:1024 nt
	global_load_dwordx2 v[22:23], v[38:39], off offset:1536 nt
	s_waitcnt lgkmcnt(0)
	v_add_f32_e32 v27, v27, v42
	v_fmamk_f32 v27, v27, 0x3a800000, v34
	v_mul_f32_e32 v38, 0x4f800000, v27
	v_cmp_gt_f32_e32 vcc, s38, v27
	s_nop 1
	v_cndmask_b32_e32 v39, v27, v38, vcc
	v_sqrt_f32_e32 v42, v39
	global_load_dword v48, v[36:37], off nt
	global_load_dword v46, v[36:37], off offset:256 nt
	global_load_dword v47, v[36:37], off offset:512 nt
	global_load_dword v45, v[36:37], off offset:768 nt
	global_load_dword v44, v[24:25], off nt
	global_load_dword v43, v[24:25], off offset:256 nt
	global_load_dword v38, v[24:25], off offset:512 nt
	global_load_dword v27, v[24:25], off offset:768 nt
	v_add_u32_e32 v24, -1, v42
	v_fma_f32 v25, -v24, v42, v39
	v_cmp_ge_f32_e64 s[0:1], 0, v25
	v_add_u32_e32 v25, 1, v42
	v_fma_f32 v36, -v25, v42, v39
	v_cndmask_b32_e64 v24, v42, v24, s[0:1]
	v_cmp_lt_f32_e64 s[0:1], 0, v36
	s_nop 1
	v_cndmask_b32_e64 v24, v24, v25, s[0:1]
	v_mul_f32_e32 v25, 0x37800000, v24
	v_cndmask_b32_e32 v24, v24, v25, vcc
	v_cmp_class_f32_e32 vcc, v39, v35
	s_nop 1
	v_cndmask_b32_e32 v55, v24, v39, vcc
	v_div_scale_f32 v57, s[0:1], v55, v55, 1.0
	v_rcp_f32_e32 v61, v57
	global_load_dword v42, v[68:69], off nt
	global_load_dword v41, v[68:69], off offset:256 nt
	global_load_dword v40, v[68:69], off offset:512 nt
	global_load_dword v39, v[68:69], off offset:768 nt
	global_load_dword v36, v[74:75], off nt
	global_load_dword v37, v[74:75], off offset:256 nt
	global_load_dword v25, v[74:75], off offset:512 nt
	global_load_dword v24, v[74:75], off offset:768 nt
	v_lshl_add_u64 v[68:69], s[10:11], 0, v[8:9]
	v_fma_f32 v66, -v57, v61, 1.0
	v_fmac_f32_e32 v61, v66, v61
	v_div_scale_f32 v66, vcc, 1.0, v55, 1.0
	v_mul_f32_e32 v70, v66, v61
	v_fma_f32 v72, -v57, v70, v66
	v_fmac_f32_e32 v70, v72, v61
	v_fma_f32 v57, -v57, v70, v66
	v_div_fmas_f32 v57, v57, v61, v70
	v_div_fixup_f32 v72, v57, v55, 1.0
	v_pk_mul_f32 v[62:63], v[72:73], v[62:63] op_sel_hi:[0,1]
	v_pk_mul_f32 v[64:65], v[72:73], v[64:65] op_sel_hi:[0,1]
	v_mov_b32_e32 v55, v26
	v_pk_mul_f32 v[58:59], v[72:73], v[58:59] op_sel_hi:[0,1]
	v_pk_mul_f32 v[54:55], v[72:73], v[54:55] op_sel_hi:[0,1]
	v_mov_b32_e32 v57, v80
	v_mov_b32_e32 v61, v90
	s_waitcnt vmcnt(20)
	v_pk_mul_f32 v[52:53], v[202:203], v[64:65]
	v_pk_mul_f32 v[50:51], v[200:201], v[62:63]
	global_store_dwordx4 v[68:69], v[50:53], off nt
	v_pk_mul_f32 v[56:57], v[72:73], v[56:57] op_sel_hi:[0,1]
	v_mov_b32_e32 v70, v49
	v_mov_b32_e32 v66, v73
	v_pk_mul_f32 v[50:51], v[204:205], v[54:55]
	v_pk_mul_f32 v[52:53], v[206:207], v[58:59]
	global_store_dwordx4 v[68:69], v[50:53], off offset:1024 nt
	v_pk_mul_f32 v[54:55], v[72:73], v[60:61] op_sel_hi:[0,1]
	s_nop 1
	v_pk_mul_f32 v[50:51], v[208:209], v[56:57]
	v_pk_mul_f32 v[52:53], v[210:211], v[54:55]
	global_store_dwordx4 v[68:69], v[50:53], off offset:2048 nt
	v_pk_mul_f32 v[54:55], v[72:73], v[66:67] op_sel_hi:[0,1]
	v_pk_mul_f32 v[56:57], v[72:73], v[70:71] op_sel_hi:[0,1]
	v_pk_mul_f32 v[50:51], v[212:213], v[54:55]
	v_pk_mul_f32 v[52:53], v[214:215], v[56:57]
	global_store_dwordx4 v[68:69], v[50:53], off offset:3072 nt
	s_waitcnt vmcnt(4)
	s_cbranch_scc1 .LBB0_1396
	s_nop 0
	v_and_b32_e32 v51, 0xffff0000, v23
	v_lshlrev_b32_e32 v53, 16, v23
	v_and_b32_e32 v49, 0xffff0000, v22
	v_lshlrev_b32_e32 v82, 16, v22
	v_cvt_pk_f32_fp8_e32 v[22:23], v46
	v_cvt_pk_f32_fp8_e32 v[66:67], v43
	v_mov_b32_e32 v70, v18
	v_mov_b32_e32 v71, v20
	v_mov_b32_e32 v73, v22
	v_mov_b32_e32 v72, v66
	v_and_b32_e32 v75, 0xffff0000, v0
	v_lshlrev_b32_e32 v0, 16, v0
	v_cvt_pk_f32_fp8_e32 v[56:57], v47
	v_cvt_pk_f32_fp8_sdwa v[58:59], v47 src0_sel:WORD_1
	v_cvt_pk_f32_fp8_sdwa v[46:47], v46 src0_sel:WORD_1
	v_cvt_pk_f32_fp8_sdwa v[68:69], v43 src0_sel:WORD_1
	v_pk_mul_f32 v[72:73], v[70:71], v[72:73]
	v_mov_b32_e32 v22, v67
	v_add_f32_e32 v0, v73, v0
	v_and_b32_e32 v26, 0xffff0000, v7
	v_lshlrev_b32_e32 v50, 16, v7
	v_and_b32_e32 v74, 0xffff0000, v6
	v_lshlrev_b32_e32 v52, 16, v6
	v_cvt_pk_f32_fp8_e32 v[6:7], v48
	v_cvt_pk_f32_fp8_sdwa v[54:55], v48 src0_sel:WORD_1
	v_add_f32_e32 v48, v72, v0
	v_pk_mul_f32 v[22:23], v[70:71], v[22:23]
	v_cvt_pk_f32_fp8_e32 v[72:73], v38
	v_add_f32_e32 v0, v23, v75
	v_add_f32_e32 v0, v22, v0
	v_mov_b32_e32 v22, v20
	v_mov_b32_e32 v23, v18
	v_mov_b32_e32 v67, v68
	v_mov_b32_e32 v68, v47
	v_cvt_pk_f32_fp8_e32 v[60:61], v45
	v_mov_b32_e32 v66, v46
	v_pk_mul_f32 v[46:47], v[22:23], v[68:69]
	v_cvt_pk_f32_fp8_sdwa v[68:69], v38 src0_sel:WORD_1
	v_fmac_f32_e32 v52, v20, v56
	v_mov_b32_e32 v56, v73
	v_pk_mul_f32 v[56:57], v[70:71], v[56:57]
	v_fmac_f32_e32 v82, v20, v60
	v_add_f32_e32 v38, v57, v74
	v_add_f32_e32 v60, v56, v38
	v_mov_b32_e32 v56, v59
	v_mov_b32_e32 v57, v69
	v_pk_mul_f32 v[66:67], v[22:23], v[66:67]
	v_pk_mul_f32 v[22:23], v[22:23], v[56:57]
	v_cvt_pk_f32_fp8_e32 v[56:57], v27
	v_cvt_pk_f32_fp8_e32 v[76:77], v39
	v_mov_b32_e32 v78, v2
	v_mov_b32_e32 v79, v18
	v_mov_b32_e32 v81, v56
	v_mov_b32_e32 v80, v76
	v_cvt_pk_f32_fp8_e32 v[70:71], v41
	v_pk_mul_f32 v[78:79], v[78:79], v[80:81]
	v_cvt_pk_f32_fp8_e32 v[80:81], v37
	v_add_f32_e32 v22, v22, v26
	v_add_f32_e32 v69, v22, v23
	v_cvt_pk_f32_fp8_sdwa v[22:23], v41 src0_sel:WORD_1
	v_add_f32_e32 v56, v79, v82
	v_cvt_pk_f32_fp8_e32 v[82:83], v36
	v_cvt_pk_f32_fp8_sdwa v[84:85], v36 src0_sel:WORD_1
	v_cvt_pk_f32_fp8_sdwa v[36:37], v37 src0_sel:WORD_1
	v_cvt_pk_f32_fp8_e32 v[74:75], v40
	v_cvt_pk_f32_fp8_e32 v[88:89], v25
	v_mov_b32_e32 v86, v81
	v_mov_b32_e32 v87, v71
	v_pk_mul_f32 v[86:87], v[2:3], v[86:87] op_sel:[1,0] op_sel_hi:[0,1]
	v_cvt_pk_f32_fp8_sdwa v[40:41], v40 src0_sel:WORD_1
	v_add_f32_e32 v0, v87, v0
	v_mov_b32_e32 v87, v22
	v_mov_b32_e32 v22, v37
	v_cvt_pk_f32_fp8_sdwa v[90:91], v25 src0_sel:WORD_1
	v_add_f32_e32 v79, v78, v56
	v_add_f32_e32 v56, v86, v0
	v_mov_b32_e32 v86, v36
	v_pk_mul_f32 v[36:37], v[2:3], v[22:23] op_sel:[1,0] op_sel_hi:[0,1]
	v_mov_b32_e32 v22, v89
	v_mov_b32_e32 v23, v75
	v_cvt_pk_f32_fp8_sdwa v[62:63], v45 src0_sel:WORD_1
	v_pk_mul_f32 v[22:23], v[2:3], v[22:23] op_sel:[1,0] op_sel_hi:[0,1]
	v_cvt_pk_f32_fp8_e32 v[64:65], v44
	v_cvt_pk_f32_fp8_sdwa v[44:45], v44 src0_sel:WORD_1
	v_cvt_pk_f32_fp8_sdwa v[26:27], v27 src0_sel:WORD_1
	v_add_f32_e32 v0, v23, v60
	v_add_f32_e32 v100, v22, v0
	v_mov_b32_e32 v22, v91
	v_mov_b32_e32 v23, v41
	v_pk_mul_f32 v[22:23], v[2:3], v[22:23] op_sel:[1,0] op_sel_hi:[0,1]
	v_lshlrev_b32_e32 v98, 16, v4
	v_and_b32_e32 v99, 0xffff0000, v4
	v_lshlrev_b32_e32 v4, 16, v5
	v_and_b32_e32 v5, 0xffff0000, v5
	v_fmac_f32_e32 v50, v20, v58
	v_add_f32_e32 v0, v69, v23
	v_pk_fma_f32 v[4:5], v[20:21], v[54:55], v[4:5] op_sel_hi:[0,1,1]
	v_mov_b32_e32 v73, v62
	v_mov_b32_e32 v69, v63
	v_cvt_pk_f32_fp8_sdwa v[38:39], v39 src0_sel:WORD_1
	v_pk_fma_f32 v[4:5], v[18:19], v[44:45], v[4:5] op_sel_hi:[0,1,1]
	v_pk_fma_f32 v[44:45], v[20:21], v[72:73], v[52:53] op_sel:[1,0,0] op_sel_hi:[0,1,1]
	v_pk_fma_f32 v[50:51], v[20:21], v[68:69], v[50:51] op_sel:[1,0,0] op_sel_hi:[0,1,1]
	v_mov_b32_e32 v52, v2
	v_mov_b32_e32 v53, v20
	v_mov_b32_e32 v71, v61
	v_mov_b32_e32 v41, v27
	v_cvt_pk_f32_fp8_sdwa v[92:93], v24 src0_sel:WORD_1
	v_cvt_pk_f32_fp8_e32 v[94:95], v24
	v_pk_fma_f32 v[6:7], v[20:21], v[6:7], v[98:99] op_sel_hi:[0,1,1]
	v_pk_fma_f32 v[20:21], v[52:53], v[70:71], v[48:49]
	v_mov_b32_e32 v75, v26
	v_pk_fma_f32 v[26:27], v[18:19], v[40:41], v[50:51] op_sel:[1,0,0] op_sel_hi:[0,1,1]
	v_mov_b32_e32 v40, v3
	v_mov_b32_e32 v41, v18
	v_mov_b32_e32 v81, v57
	v_pk_mul_f32 v[76:77], v[2:3], v[76:77] op_sel:[1,0] op_sel_hi:[0,1]
	v_pk_fma_f32 v[6:7], v[18:19], v[64:65], v[6:7] op_sel_hi:[0,1,1]
	v_pk_fma_f32 v[44:45], v[18:19], v[74:75], v[44:45] op_sel:[1,0,0] op_sel_hi:[0,1,1]
	v_pk_fma_f32 v[18:19], v[40:41], v[80:81], v[20:21]
	v_mov_b32_e32 v89, v38
	v_mov_b32_e32 v76, v18
	v_mov_b32_e32 v91, v39
	v_pk_mul_f32 v[38:39], v[18:19], v[18:19]
	v_pk_add_f32 v[40:41], v[18:19], v[76:77]
	v_cvt_pk_f32_fp8_e32 v[58:59], v42
	v_cvt_pk_f32_fp8_sdwa v[42:43], v42 src0_sel:WORD_1
	v_pk_mul_f32 v[96:97], v[2:3], v[92:93] op_sel:[1,0] op_sel_hi:[0,1]
	v_pk_fma_f32 v[20:21], v[2:3], v[88:89], v[44:45] op_sel:[1,0,0] op_sel_hi:[0,1,1]
	v_mov_b32_e32 v39, v41
	v_mov_b32_e32 v57, v3
	v_mov_b32_e32 v44, v56
	v_mov_b32_e32 v45, v95
	v_pk_mul_f32 v[92:93], v[2:3], v[92:93]
	v_pk_fma_f32 v[26:27], v[2:3], v[90:91], v[26:27] op_sel:[1,0,0] op_sel_hi:[0,1,1]
	v_pk_fma_f32 v[38:39], v[56:57], v[44:45], v[38:39]
	v_mov_b32_e32 v44, v20
	v_mov_b32_e32 v45, v96
	v_add_f32_e32 v101, v0, v22
	v_mul_f32_e32 v0, v100, v100
	v_pk_add_f32 v[44:45], v[20:21], v[44:45]
	v_mov_b32_e32 v92, v26
	v_mul_f32_e32 v60, v101, v101
	v_pk_add_f32 v[48:49], v[26:27], v[92:93]
	v_pk_fma_f32 v[50:51], v[20:21], v[20:21], v[0:1]
	v_pk_mul_f32 v[52:53], v[44:45], v[44:45]
	v_pk_fma_f32 v[6:7], v[2:3], v[58:59], v[6:7] op_sel_hi:[0,1,1]
	v_pk_fma_f32 v[4:5], v[2:3], v[42:43], v[4:5] op_sel_hi:[0,1,1]
	v_mov_b32_e32 v51, v53
	v_pk_fma_f32 v[52:53], v[26:27], v[26:27], v[60:61]
	v_pk_mul_f32 v[54:55], v[48:49], v[48:49]
	v_pk_fma_f32 v[6:7], v[2:3], v[82:83], v[6:7] op_sel:[1,0,0]
	v_pk_fma_f32 v[4:5], v[2:3], v[84:85], v[4:5] op_sel:[1,0,0]
	v_mov_b32_e32 v53, v55
	v_pk_mul_f32 v[86:87], v[2:3], v[86:87] op_sel:[1,0] op_sel_hi:[0,1]
	v_pk_mul_f32 v[42:43], v[4:5], v[4:5]
	v_pk_add_f32 v[50:51], v[50:51], v[52:53]
	v_mov_b32_e32 v2, v6
	v_mov_b32_e32 v52, v6
	v_mov_b32_e32 v53, v94
	v_mul_f32_e32 v78, v7, v7
	v_mov_b32_e32 v54, v4
	v_mov_b32_e32 v55, v3
	v_mov_b32_e32 v58, v4
	v_mov_b32_e32 v59, v94
	v_pk_fma_f32 v[52:53], v[2:3], v[52:53], v[78:79]
	v_mov_b32_e32 v78, v43
	v_pk_fma_f32 v[42:43], v[54:55], v[58:59], v[78:79]
	v_pk_add_f32 v[54:55], v[52:53], v[42:43]
	v_pk_mul_f32 v[42:43], v[52:53], v[42:43]
	v_lshlrev_b32_e32 v0, 16, v1
	v_mov_b32_e32 v55, v43
	v_and_b32_e32 v1, 0xffff0000, v1
	v_mov_b32_e32 v42, v66
	v_mov_b32_e32 v43, v46
	v_pk_add_f32 v[0:1], v[42:43], v[0:1]
	v_mov_b32_e32 v46, v67
	v_pk_add_f32 v[0:1], v[0:1], v[46:47]
	v_mov_b32_e32 v42, v87
	v_mov_b32_e32 v43, v37
	v_pk_add_f32 v[0:1], v[0:1], v[42:43]
	v_mov_b32_e32 v87, v36
	v_pk_add_f32 v[36:37], v[0:1], v[86:87]
	v_mov_b32_e32 v27, v101
	v_pk_mul_f32 v[0:1], v[36:37], v[36:37]
	v_mov_b32_e32 v2, v37
	v_mov_b32_e32 v94, v37
	v_mov_b32_e32 v1, v41
	v_pk_fma_f32 v[0:1], v[2:3], v[94:95], v[0:1]
	v_lshl_add_u64 v[40:41], s[6:7], 0, v[8:9]
	v_pk_add_f32 v[2:3], v[38:39], v[0:1]
	v_pk_mul_f32 v[0:1], v[38:39], v[0:1]
	v_mov_b32_e32 v48, v45
	v_mov_b32_e32 v3, v1
	v_pk_add_f32 v[0:1], v[54:55], v[2:3]
	v_mov_b32_e32 v38, v53
	v_pk_add_f32 v[0:1], v[0:1], v[50:51]
	s_nop 0
	v_add_f32_e32 v0, v0, v1
	ds_bpermute_b32 v1, v28, v0
	s_waitcnt lgkmcnt(0)
	v_add_f32_e32 v0, v0, v1
	ds_bpermute_b32 v1, v29, v0
	s_waitcnt lgkmcnt(0)
	v_add_f32_e32 v0, v0, v1
	ds_bpermute_b32 v1, v30, v0
	s_waitcnt lgkmcnt(0)
	v_add_f32_e32 v0, v0, v1
	ds_bpermute_b32 v1, v31, v0
	s_waitcnt lgkmcnt(0)
	v_add_f32_e32 v0, v0, v1
	ds_bpermute_b32 v1, v32, v0
	s_waitcnt lgkmcnt(0)
	v_add_f32_e32 v0, v0, v1
	ds_bpermute_b32 v1, v33, v0
	s_waitcnt lgkmcnt(0)
	v_add_f32_e32 v0, v0, v1
	v_fmamk_f32 v0, v0, 0x3a800000, v34
	v_mul_f32_e32 v1, 0x4f800000, v0
	v_cmp_gt_f32_e32 vcc, s38, v0
	s_nop 1
	v_cndmask_b32_e32 v0, v0, v1, vcc
	v_sqrt_f32_e32 v1, v0
	s_nop 0
	v_add_u32_e32 v2, -1, v1
	v_fma_f32 v3, -v2, v1, v0
	v_cmp_ge_f32_e64 s[0:1], 0, v3
	v_add_u32_e32 v3, 1, v1
	s_nop 0
	v_cndmask_b32_e64 v2, v1, v2, s[0:1]
	v_fma_f32 v1, -v3, v1, v0
	v_cmp_lt_f32_e64 s[0:1], 0, v1
	s_nop 1
	v_cndmask_b32_e64 v1, v2, v3, s[0:1]
	v_mul_f32_e32 v2, 0x37800000, v1
	v_cndmask_b32_e32 v1, v1, v2, vcc
	v_cmp_class_f32_e32 vcc, v0, v35
	s_nop 1
	v_cndmask_b32_e32 v0, v1, v0, vcc
	v_div_scale_f32 v1, s[0:1], v0, v0, 1.0
	v_rcp_f32_e32 v2, v1
	s_nop 0
	v_fma_f32 v3, -v1, v2, 1.0
	v_fmac_f32_e32 v2, v3, v2
	v_div_scale_f32 v3, vcc, 1.0, v0, 1.0
	v_mul_f32_e32 v19, v3, v2
	v_fma_f32 v21, -v1, v19, v3
	v_fmac_f32_e32 v19, v21, v2
	v_fma_f32 v1, -v1, v19, v3
	v_div_fmas_f32 v1, v1, v2, v19
	v_div_fixup_f32 v42, v1, v0, 1.0
	v_pk_mul_f32 v[0:1], v[42:43], v[6:7] op_sel_hi:[0,1]
	v_pk_mul_f32 v[2:3], v[42:43], v[4:5] op_sel_hi:[0,1]
	s_waitcnt vmcnt(4)
	v_pk_mul_f32 v[2:3], v[202:203], v[2:3]
	v_pk_mul_f32 v[0:1], v[200:201], v[0:1]
	global_store_dwordx4 v[40:41], v[0:3], off nt
	v_mov_b32_e32 v19, v56
	v_pk_mul_f32 v[4:5], v[42:43], v[36:37] op_sel_hi:[0,1]
	v_pk_mul_f32 v[6:7], v[42:43], v[18:19] op_sel_hi:[0,1]
	v_mov_b32_e32 v21, v100
	v_pk_mul_f32 v[0:1], v[204:205], v[6:7]
	v_pk_mul_f32 v[2:3], v[206:207], v[4:5]
	global_store_dwordx4 v[40:41], v[0:3], off offset:1024 nt
	v_pk_mul_f32 v[4:5], v[42:43], v[26:27] op_sel_hi:[0,1]
	v_pk_mul_f32 v[6:7], v[42:43], v[20:21] op_sel_hi:[0,1]
	v_pk_mul_f32 v[0:1], v[208:209], v[6:7]
	v_pk_mul_f32 v[2:3], v[210:211], v[4:5]
	global_store_dwordx4 v[40:41], v[0:3], off offset:2048 nt
	v_pk_mul_f32 v[4:5], v[42:43], v[38:39] op_sel_hi:[0,1]
	v_pk_mul_f32 v[6:7], v[42:43], v[48:49] op_sel_hi:[0,1]
	v_pk_mul_f32 v[0:1], v[212:213], v[4:5]
	v_pk_mul_f32 v[2:3], v[214:215], v[6:7]
	global_store_dwordx4 v[40:41], v[0:3], off offset:3072 nt
	s_branch .LBB0_1396
